# v39 + attention->out-projection grid barriers replaced by hand-offs among the 32 workgroups of one batch element
# speedup vs baseline: 1.0079x; 1.0079x over previous
; __device__ __forceinline__ unsigned xb_ld(unsigned* p)              { return __hip_atomic_load(p, __ATOMIC_RELAXED, __HIP_MEMORY_SCOPE_AGENT); }
; __device__ __forceinline__ unsigned xb_add(unsigned* p, unsigned v) { return __hip_atomic_fetch_add(p, v, __ATOMIC_RELAXED, __HIP_MEMORY_SCOPE_AGENT); }
; #define XB_SPIN(cond, bar) do { unsigned _sp = 0; while (cond) { __builtin_amdgcn_s_sleep(1); \
;     if ((++_sp & 255u) == 0u) { if (xb_ld(&(bar)[XB_TMO])) break; if (_sp > XB_SPIN_CAP) { atomicAdd(&(bar)[XB_TMO], 1u); break; } } } } while (0)
; __device__ __forceinline__ void xcd_barrier(const XcdBarrier& b) {
;     asm volatile("s_waitcnt vmcnt(0)" ::: "memory");
;     __syncthreads();
;     if (threadIdx.x == 0) {
;         unsigned* bar = b.bar;
;         __builtin_amdgcn_s_waitcnt(0);
;         unsigned nloc = b.st[0], nx = b.st[1];
;         if (nloc == 0u) { xcd_barrier_complete(bar, b.x, nloc, nx); b.st[0] = nloc; b.st[1] = nx; }
;         const unsigned old = xb_add(&bar[XB_XSUB(b.x)], 1u);
;         const unsigned gen = old / nloc;
;         if (old + 1u == (gen + 1u) * nloc) {
;             __builtin_amdgcn_fence(__ATOMIC_RELEASE, "agent");
;             asm volatile("s_waitcnt vmcnt(0)" ::: "memory");
;             const unsigned og = xb_add(&bar[XB_TOP], 1u);
;             const unsigned tg = og / nx;
;             if (og + 1u == (tg + 1u) * nx) xb_add(&bar[XB_TOPGEN], 1u);
;             else XB_SPIN(xb_ld(&bar[XB_TOPGEN]) == tg, bar);
;             __builtin_amdgcn_fence(__ATOMIC_ACQUIRE, "agent");
;             xb_add(&bar[XB_XGEN(b.x)], 1u);
;             asm volatile("s_waitcnt vmcnt(0)" ::: "memory");
;         } else {
;             XB_SPIN(xb_ld(&bar[XB_XGEN(b.x)]) == gen, bar);
;             __builtin_amdgcn_fence(__ATOMIC_ACQUIRE, "agent");
;             asm volatile("s_waitcnt vmcnt(0)" ::: "memory");
;         }
;     }
;     __syncthreads();
; }
.LBB0_1027:
	v_readlane_b32 s0, v253, 42
	v_readlane_b32 s4, v253, 32
	s_add_i32 s0, s0, 5
	v_readlane_b32 s7, v253, 35
	s_cmp_ge_i32 s0, s7
	v_readlane_b32 s5, v253, 33
	v_readlane_b32 s6, v253, 34
	s_cbranch_scc1 .LBB0_1073
	v_readlane_b32 s38, v253, 36
	v_readlane_b32 s39, v253, 37
	s_mov_b32 s1, s76
	s_waitcnt vmcnt(0)
	s_waitcnt vmcnt(0)
	s_barrier
	s_mov_b64 s[40:41], exec
	v_readlane_b32 s4, v253, 53
	v_readlane_b32 s5, v253, 54
	s_and_b64 s[4:5], s[40:41], s[4:5]
	s_mov_b64 exec, s[4:5]
	s_cbranch_execz .LBB0_1072
	v_readlane_b32 s10, v253, 36
	v_readlane_b32 s11, v253, 37
	v_readlane_b32 s14, v253, 55
	s_nop 3
	s_add_u32 s12, s10, 0x8000
	s_addc_u32 s13, s11, 0
	s_and_b32 s15, s88, 7
	s_lshl_b32 s15, s15, 8
	s_lshr_b32 s14, s14, 2
	s_add_i32 s14, s14, 1
	s_lshl_b32 s14, s14, 5
	v_mov_b32_e32 v2, s15
	v_mov_b32_e32 v5, 1
	global_atomic_add v2, v5, s[12:13]
	s_mov_b32 s18, 0

; __device__ __forceinline__ unsigned xb_ld(unsigned* p)              { return __hip_atomic_load(p, __ATOMIC_RELAXED, __HIP_MEMORY_SCOPE_AGENT); }
; __device__ __forceinline__ unsigned xb_add(unsigned* p, unsigned v) { return __hip_atomic_fetch_add(p, v, __ATOMIC_RELAXED, __HIP_MEMORY_SCOPE_AGENT); }
; #define XB_SPIN(cond, bar) do { unsigned _sp = 0; while (cond) { __builtin_amdgcn_s_sleep(1); \
;     if ((++_sp & 255u) == 0u) { if (xb_ld(&(bar)[XB_TMO])) break; if (_sp > XB_SPIN_CAP) { atomicAdd(&(bar)[XB_TMO], 1u); break; } } } } while (0)
; __device__ __forceinline__ void xcd_barrier(const XcdBarrier& b) {
;     asm volatile("s_waitcnt vmcnt(0)" ::: "memory");
;     __syncthreads();
;     if (threadIdx.x == 0) {
;         unsigned* bar = b.bar;
;         __builtin_amdgcn_s_waitcnt(0);
;         unsigned nloc = b.st[0], nx = b.st[1];
;         if (nloc == 0u) { xcd_barrier_complete(bar, b.x, nloc, nx); b.st[0] = nloc; b.st[1] = nx; }
;         const unsigned old = xb_add(&bar[XB_XSUB(b.x)], 1u);
;         const unsigned gen = old / nloc;
;         if (old + 1u == (gen + 1u) * nloc) {
;             __builtin_amdgcn_fence(__ATOMIC_RELEASE, "agent");
;             asm volatile("s_waitcnt vmcnt(0)" ::: "memory");
;             const unsigned og = xb_add(&bar[XB_TOP], 1u);
;             const unsigned tg = og / nx;
;             if (og + 1u == (tg + 1u) * nx) xb_add(&bar[XB_TOPGEN], 1u);
;             else XB_SPIN(xb_ld(&bar[XB_TOPGEN]) == tg, bar);
;             __builtin_amdgcn_fence(__ATOMIC_ACQUIRE, "agent");
;             xb_add(&bar[XB_XGEN(b.x)], 1u);
;             asm volatile("s_waitcnt vmcnt(0)" ::: "memory");
;         } else {
;             XB_SPIN(xb_ld(&bar[XB_XGEN(b.x)]) == gen, bar);
;             __builtin_amdgcn_fence(__ATOMIC_ACQUIRE, "agent");
;             asm volatile("s_waitcnt vmcnt(0)" ::: "memory");
;         }
;     }
;     __syncthreads();
; }
.LBB0_1627:
	v_readlane_b32 s0, v253, 42
	v_readlane_b32 s4, v253, 32
	s_add_i32 s0, s0, 7
	v_readlane_b32 s7, v253, 35
	s_cmp_ge_i32 s0, s7
	v_readlane_b32 s5, v253, 33
	v_readlane_b32 s6, v253, 34
	s_cbranch_scc1 .LBB0_1673
	v_readlane_b32 s34, v253, 36
	v_readlane_b32 s35, v253, 37
	s_mov_b32 s1, s76
	s_waitcnt vmcnt(0)
	s_waitcnt vmcnt(0) lgkmcnt(0)
	s_barrier
	s_mov_b64 s[36:37], exec
	v_readlane_b32 s2, v253, 53
	v_readlane_b32 s3, v253, 54
	s_and_b64 s[2:3], s[36:37], s[2:3]
	s_mov_b64 exec, s[2:3]
	s_cbranch_execz .LBB0_1672
	v_readlane_b32 s10, v253, 36
	v_readlane_b32 s11, v253, 37
	v_readlane_b32 s14, v253, 55
	s_nop 3
	s_add_u32 s12, s10, 0x8800
	s_addc_u32 s13, s11, 0
	s_and_b32 s15, s88, 7
	s_lshl_b32 s15, s15, 8
	s_lshr_b32 s14, s14, 2
	s_add_i32 s14, s14, 1
	s_lshl_b32 s14, s14, 5
	v_mov_b32_e32 v2, s15
	v_mov_b32_e32 v5, 1
	global_atomic_add v2, v5, s[12:13]
	s_mov_b32 s18, 0
